# prologue: the 8 context hyena tasks run on workgroups 192,200,...,248 (no modulation-vector task there) under the rotated task index
# speedup vs baseline: 1.0050x; 1.0050x over previous
;     ...
;     ((float*)(P.ws + WS_NORMP))[(size_t)tid * 520 + task] = asum;
;     ...
;         for (int task = bid; task < 520; task += nb) hyena_filter_task(P, sm, task, rep == 0 ? 1 : 0);
.LBB0_36:
	s_ashr_i32 s15, s14, 31
	v_readlane_b32 s0, v253, 10
	v_lshl_add_u64 v[2:3], s[14:15], 2, v[14:15]
	v_readlane_b32 s1, v253, 11
	global_store_dword v[2:3], v22, off
	s_add_i32 s14, s14, s0
	s_cmpk_lg_u32 s0, 0x100
	s_cbranch_scc1 .Lhyd_orig
	s_cmpk_lt_i32 s14, 0x200
	s_cbranch_scc1 .LBB0_37
	s_addk_i32 s14, 0xffe8
	s_cmpk_lt_i32 s14, 0x200
	s_cbranch_scc1 .LBB0_109
